# v25 = v24 + in0/in1 converter-workgroup stores at default cache policy
# speedup vs baseline: 1.0150x; 1.0058x over previous
; __device__ __forceinline__ ConvTile conv_tile_desc(const unsigned long long* tab, int t) {
;     ...
;     else { const int u = (t < CT_TOTAL ? t : CT_TOTAL - 1) - CT_C; e = u / 7168; const int v = u % 7168; si = 9; di = 17; N = DM; K = EXD; nb = v & 31; kb = v >> 5; }
;     const int n0 = nb * 64;
;     int col0 = n0, nvalid = 64;
;     if (mode) { col0 = (n0 >> 8) * 128 + (n0 & 127); si += (n0 >> 7) & 1; }
;     if (npad) { nvalid = N - n0; if (nvalid <= 0) col0 = 0; }
;     ConvTile c;
;     const size_t KN = (size_t)K * N;
;     c.src = (const float*)tab[si] + (size_t)e * KN + (size_t)(kb * 32) * N + col0;
;     c.dst = (bf16_t*)tab[di] + (size_t)e * (mode ? 2 * KN : KN) + (size_t)n0 * K + kb * 32;
;     c.N = N; c.K = K; c.nvalid = nvalid;
;     return c;
; }
.Lcv0_start:
	v_and_b32_e32 v96, 63, v0
	v_lshrrev_b32_e32 v97, 6, v0
	v_lshrrev_b32_e32 v98, 4, v96
	v_and_b32_e32 v99, 15, v96
	v_readfirstlane_b32 s2, v97
	v_lshlrev_b32_e32 v100, 16, v98
	v_lshl_add_u32 v100, v99, 4, v100
	v_add_u32_e32 v101, 0x2000, v100
	v_add_u32_e32 v102, 0x4000, v100
	v_add_u32_e32 v103, 0x6000, v100
	v_add_u32_e32 v104, 0x8000, v100
	v_add_u32_e32 v105, 0xa000, v100
	v_add_u32_e32 v106, 0xc000, v100
	v_add_u32_e32 v107, 0xe000, v100
	v_mul_u32_u24_e32 v108, 0xe000, v99
	v_lshl_add_u32 v108, v98, 4, v108
	v_add_u32_e32 v109, 0x3800, v108
	v_add_u32_e32 v110, 0x7000, v108
	v_add_u32_e32 v111, 0xa800, v108
	v_mov_b32_e32 v112, 0x20088
	v_mov_b32_e32 v113, 0x200c8
	ds_read_b64 v[114:115], v112
	ds_read_b64 v[116:117], v113
	s_waitcnt lgkmcnt(0)
	v_readfirstlane_b32 s4, v114
	v_readfirstlane_b32 s5, v115
	v_readfirstlane_b32 s6, v116
	v_readfirstlane_b32 s7, v117
	s_sub_i32 s3, s90, 224
	s_lshl_b32 s3, s3, 3
	s_add_i32 s3, s3, s2
	s_add_i32 s3, s3, 0x2ac00
	s_nop 4
	s_min_u32 s12, s3, 0x324ff
	s_sub_u32 s12, s12, 0x24500
	s_lshr_b32 s13, s12, 10
	s_mul_i32 s13, s13, 37
	s_lshr_b32 s13, s13, 8
	s_mul_i32 s28, s13, 0x1c00
	s_sub_u32 s12, s12, s28
	s_bfe_u32 s28, s12, 0x50001
	s_and_b32 s32, s12, 1
	s_lshr_b32 s12, s12, 6
	s_lshl_b32 s12, s12, 1
	s_or_b32 s12, s12, s32
	s_mul_i32 s29, s13, 0x3800000
	s_lshl_b32 s32, s12, 18
	s_add_u32 s29, s29, s32
	s_lshl_b32 s32, s28, 8
	s_add_u32 s29, s29, s32
	s_add_u32 s8, s4, s29
	s_addc_u32 s9, s5, 0
	s_mul_i32 s29, s13, 0x1c00000
	s_mul_i32 s32, s28, 0xe0000
	s_add_u32 s29, s29, s32
	s_lshl_b32 s32, s12, 6
	s_add_u32 s29, s29, s32
	s_add_u32 s10, s6, s29
	s_addc_u32 s11, s7, 0
	s_nop 0
	global_load_dwordx4 v[128:131], v100, s[8:9] nt
	global_load_dwordx4 v[132:135], v101, s[8:9] nt
	global_load_dwordx4 v[136:139], v102, s[8:9] nt
	global_load_dwordx4 v[140:143], v103, s[8:9] nt
	global_load_dwordx4 v[144:147], v104, s[8:9] nt
	global_load_dwordx4 v[148:151], v105, s[8:9] nt
	global_load_dwordx4 v[152:155], v106, s[8:9] nt
	global_load_dwordx4 v[156:159], v107, s[8:9] nt
	s_add_i32 s3, s3, 256
	s_min_u32 s12, s3, 0x324ff
	s_sub_u32 s12, s12, 0x24500
	s_lshr_b32 s13, s12, 10
	s_mul_i32 s13, s13, 37
	s_lshr_b32 s13, s13, 8
	s_mul_i32 s28, s13, 0x1c00
	s_sub_u32 s12, s12, s28
	s_bfe_u32 s28, s12, 0x50001
	s_and_b32 s32, s12, 1
	s_lshr_b32 s12, s12, 6
	s_lshl_b32 s12, s12, 1
	s_or_b32 s12, s12, s32
	s_mul_i32 s29, s13, 0x3800000
	s_lshl_b32 s32, s12, 18
	s_add_u32 s29, s29, s32
	s_lshl_b32 s32, s28, 8
	s_add_u32 s29, s29, s32
	s_add_u32 s8, s4, s29
	s_addc_u32 s9, s5, 0
	s_mul_i32 s29, s13, 0x1c00000
	s_mul_i32 s32, s28, 0xe0000
	s_add_u32 s29, s29, s32
	s_lshl_b32 s32, s12, 6
	s_add_u32 s29, s29, s32
	s_add_u32 s36, s6, s29
	s_addc_u32 s37, s7, 0
	s_nop 0
	global_load_dwordx4 v[64:67], v100, s[8:9] nt
	global_load_dwordx4 v[68:71], v101, s[8:9] nt
	global_load_dwordx4 v[72:75], v102, s[8:9] nt
	global_load_dwordx4 v[76:79], v103, s[8:9] nt
	global_load_dwordx4 v[80:83], v104, s[8:9] nt
	global_load_dwordx4 v[84:87], v105, s[8:9] nt
	global_load_dwordx4 v[88:91], v106, s[8:9] nt
	global_load_dwordx4 v[92:95], v107, s[8:9] nt
	s_waitcnt vmcnt(8)
	v_cvt_pk_bf16_f32 v112, v128, v132
	v_cvt_pk_bf16_f32 v113, v136, v140
	v_cvt_pk_bf16_f32 v114, v144, v148
	v_cvt_pk_bf16_f32 v115, v152, v156
	global_store_dwordx4 v108, v[112:115], s[10:11]
	v_cvt_pk_bf16_f32 v116, v129, v133
	v_cvt_pk_bf16_f32 v117, v137, v141
	v_cvt_pk_bf16_f32 v118, v145, v149
	v_cvt_pk_bf16_f32 v119, v153, v157
	global_store_dwordx4 v109, v[116:119], s[10:11]
	v_cvt_pk_bf16_f32 v120, v130, v134
	v_cvt_pk_bf16_f32 v121, v138, v142
	v_cvt_pk_bf16_f32 v122, v146, v150
	v_cvt_pk_bf16_f32 v123, v154, v158
	global_store_dwordx4 v110, v[120:123], s[10:11]
	v_cvt_pk_bf16_f32 v96, v131, v135
	v_cvt_pk_bf16_f32 v97, v139, v143
	v_cvt_pk_bf16_f32 v98, v147, v151
	v_cvt_pk_bf16_f32 v99, v155, v159
	global_store_dwordx4 v111, v[96:99], s[10:11]
	s_movk_i32 s33, 27
; __device__ __forceinline__ ConvTile conv_tile_desc(const unsigned long long* tab, int t) {
;     ...
;     else { const int u = (t < CT_TOTAL ? t : CT_TOTAL - 1) - CT_C; e = u / 7168; const int v = u % 7168; si = 9; di = 17; N = DM; K = EXD; nb = v & 31; kb = v >> 5; }
;     const int n0 = nb * 64;
;     int col0 = n0, nvalid = 64;
;     if (mode) { col0 = (n0 >> 8) * 128 + (n0 & 127); si += (n0 >> 7) & 1; }
;     if (npad) { nvalid = N - n0; if (nvalid <= 0) col0 = 0; }
;     ConvTile c;
;     const size_t KN = (size_t)K * N;
;     c.src = (const float*)tab[si] + (size_t)e * KN + (size_t)(kb * 32) * N + col0;
;     c.dst = (bf16_t*)tab[di] + (size_t)e * (mode ? 2 * KN : KN) + (size_t)n0 * K + kb * 32;
;     c.N = N; c.K = K; c.nvalid = nvalid;
;     return c;
; }
.Lcv0_loop:
	s_add_i32 s3, s3, 256
	s_min_u32 s12, s3, 0x324ff
	s_sub_u32 s12, s12, 0x24500
	s_lshr_b32 s13, s12, 10
	s_mul_i32 s13, s13, 37
	s_lshr_b32 s13, s13, 8
	s_mul_i32 s28, s13, 0x1c00
	s_sub_u32 s12, s12, s28
	s_bfe_u32 s28, s12, 0x50001
	s_and_b32 s32, s12, 1
	s_lshr_b32 s12, s12, 6
	s_lshl_b32 s12, s12, 1
	s_or_b32 s12, s12, s32
	s_mul_i32 s29, s13, 0x3800000
	s_lshl_b32 s32, s12, 18
	s_add_u32 s29, s29, s32
	s_lshl_b32 s32, s28, 8
	s_add_u32 s29, s29, s32
	s_add_u32 s8, s4, s29
	s_addc_u32 s9, s5, 0
	s_mul_i32 s29, s13, 0x1c00000
	s_mul_i32 s32, s28, 0xe0000
	s_add_u32 s29, s29, s32
	s_lshl_b32 s32, s12, 6
	s_add_u32 s29, s29, s32
	s_add_u32 s10, s6, s29
	s_addc_u32 s11, s7, 0
	s_nop 0
	global_load_dwordx4 v[128:131], v100, s[8:9] nt
	global_load_dwordx4 v[132:135], v101, s[8:9] nt
	global_load_dwordx4 v[136:139], v102, s[8:9] nt
	global_load_dwordx4 v[140:143], v103, s[8:9] nt
	global_load_dwordx4 v[144:147], v104, s[8:9] nt
	global_load_dwordx4 v[148:151], v105, s[8:9] nt
	global_load_dwordx4 v[152:155], v106, s[8:9] nt
	global_load_dwordx4 v[156:159], v107, s[8:9] nt
	s_waitcnt vmcnt(12)
	v_cvt_pk_bf16_f32 v112, v64, v68
	v_cvt_pk_bf16_f32 v113, v72, v76
	v_cvt_pk_bf16_f32 v114, v80, v84
	v_cvt_pk_bf16_f32 v115, v88, v92
	global_store_dwordx4 v108, v[112:115], s[36:37]
	v_cvt_pk_bf16_f32 v116, v65, v69
	v_cvt_pk_bf16_f32 v117, v73, v77
	v_cvt_pk_bf16_f32 v118, v81, v85
	v_cvt_pk_bf16_f32 v119, v89, v93
	global_store_dwordx4 v109, v[116:119], s[36:37]
	v_cvt_pk_bf16_f32 v120, v66, v70
	v_cvt_pk_bf16_f32 v121, v74, v78
	v_cvt_pk_bf16_f32 v122, v82, v86
	v_cvt_pk_bf16_f32 v123, v90, v94
	global_store_dwordx4 v110, v[120:123], s[36:37]
	v_cvt_pk_bf16_f32 v96, v67, v71
	v_cvt_pk_bf16_f32 v97, v75, v79
	v_cvt_pk_bf16_f32 v98, v83, v87
	v_cvt_pk_bf16_f32 v99, v91, v95
	global_store_dwordx4 v111, v[96:99], s[36:37]
	s_add_i32 s3, s3, 256
	s_min_u32 s12, s3, 0x324ff
	s_sub_u32 s12, s12, 0x24500
	s_lshr_b32 s13, s12, 10
	s_mul_i32 s13, s13, 37
	s_lshr_b32 s13, s13, 8
	s_mul_i32 s28, s13, 0x1c00
	s_sub_u32 s12, s12, s28
	s_bfe_u32 s28, s12, 0x50001
	s_and_b32 s32, s12, 1
	s_lshr_b32 s12, s12, 6
	s_lshl_b32 s12, s12, 1
	s_or_b32 s12, s12, s32
	s_mul_i32 s29, s13, 0x3800000
	s_lshl_b32 s32, s12, 18
	s_add_u32 s29, s29, s32
	s_lshl_b32 s32, s28, 8
	s_add_u32 s29, s29, s32
	s_add_u32 s8, s4, s29
	s_addc_u32 s9, s5, 0
	s_mul_i32 s29, s13, 0x1c00000
	s_mul_i32 s32, s28, 0xe0000
	s_add_u32 s29, s29, s32
	s_lshl_b32 s32, s12, 6
	s_add_u32 s29, s29, s32
	s_add_u32 s36, s6, s29
	s_addc_u32 s37, s7, 0
	s_nop 0
	global_load_dwordx4 v[64:67], v100, s[8:9] nt
	global_load_dwordx4 v[68:71], v101, s[8:9] nt
	global_load_dwordx4 v[72:75], v102, s[8:9] nt
	global_load_dwordx4 v[76:79], v103, s[8:9] nt
	global_load_dwordx4 v[80:83], v104, s[8:9] nt
	global_load_dwordx4 v[84:87], v105, s[8:9] nt
	global_load_dwordx4 v[88:91], v106, s[8:9] nt
	global_load_dwordx4 v[92:95], v107, s[8:9] nt
	s_waitcnt vmcnt(12)
	v_cvt_pk_bf16_f32 v112, v128, v132
	v_cvt_pk_bf16_f32 v113, v136, v140
	v_cvt_pk_bf16_f32 v114, v144, v148
	v_cvt_pk_bf16_f32 v115, v152, v156
	global_store_dwordx4 v108, v[112:115], s[10:11]
	v_cvt_pk_bf16_f32 v116, v129, v133
	v_cvt_pk_bf16_f32 v117, v137, v141
	v_cvt_pk_bf16_f32 v118, v145, v149
	v_cvt_pk_bf16_f32 v119, v153, v157
	global_store_dwordx4 v109, v[116:119], s[10:11]
	v_cvt_pk_bf16_f32 v120, v130, v134
	v_cvt_pk_bf16_f32 v121, v138, v142
	v_cvt_pk_bf16_f32 v122, v146, v150
	v_cvt_pk_bf16_f32 v123, v154, v158
	global_store_dwordx4 v110, v[120:123], s[10:11]
	v_cvt_pk_bf16_f32 v96, v131, v135
	v_cvt_pk_bf16_f32 v97, v139, v143
	v_cvt_pk_bf16_f32 v98, v147, v151
	v_cvt_pk_bf16_f32 v99, v155, v159
	global_store_dwordx4 v111, v[96:99], s[10:11]
	s_sub_i32 s33, s33, 1
	s_cmp_lg_u32 s33, 0
	s_cbranch_scc1 .Lcv0_loop
	s_waitcnt vmcnt(4)
	v_cvt_pk_bf16_f32 v112, v64, v68
	v_cvt_pk_bf16_f32 v113, v72, v76
	v_cvt_pk_bf16_f32 v114, v80, v84
	v_cvt_pk_bf16_f32 v115, v88, v92
	global_store_dwordx4 v108, v[112:115], s[36:37]
	v_cvt_pk_bf16_f32 v116, v65, v69
	v_cvt_pk_bf16_f32 v117, v73, v77
	v_cvt_pk_bf16_f32 v118, v81, v85
	v_cvt_pk_bf16_f32 v119, v89, v93
	global_store_dwordx4 v109, v[116:119], s[36:37]
	v_cvt_pk_bf16_f32 v120, v66, v70
	v_cvt_pk_bf16_f32 v121, v74, v78
	v_cvt_pk_bf16_f32 v122, v82, v86
	v_cvt_pk_bf16_f32 v123, v90, v94
	global_store_dwordx4 v110, v[120:123], s[36:37]
	v_cvt_pk_bf16_f32 v96, v67, v71
	v_cvt_pk_bf16_f32 v97, v75, v79
	v_cvt_pk_bf16_f32 v98, v83, v87
	v_cvt_pk_bf16_f32 v99, v91, v95
	global_store_dwordx4 v111, v[96:99], s[36:37]
	s_branch .LBB0_237

; __device__ __forceinline__ ConvTile conv_tile_desc(const unsigned long long* tab, int t) {
;     ...
;     else { const int u = (t < CT_TOTAL ? t : CT_TOTAL - 1) - CT_C; e = u / 7168; const int v = u % 7168; si = 9; di = 17; N = DM; K = EXD; nb = v & 31; kb = v >> 5; }
;     const int n0 = nb * 64;
;     int col0 = n0, nvalid = 64;
;     if (mode) { col0 = (n0 >> 8) * 128 + (n0 & 127); si += (n0 >> 7) & 1; }
;     if (npad) { nvalid = N - n0; if (nvalid <= 0) col0 = 0; }
;     ConvTile c;
;     const size_t KN = (size_t)K * N;
;     c.src = (const float*)tab[si] + (size_t)e * KN + (size_t)(kb * 32) * N + col0;
;     c.dst = (bf16_t*)tab[di] + (size_t)e * (mode ? 2 * KN : KN) + (size_t)n0 * K + kb * 32;
;     c.N = N; c.K = K; c.nvalid = nvalid;
;     return c;
; }
.Lcv1_start:
	v_and_b32_e32 v96, 63, v0
	v_lshrrev_b32_e32 v97, 6, v0
	v_lshrrev_b32_e32 v98, 4, v96
	v_and_b32_e32 v99, 15, v96
	v_readfirstlane_b32 s2, v97
	v_lshlrev_b32_e32 v100, 16, v98
	v_lshl_add_u32 v100, v99, 4, v100
	v_add_u32_e32 v101, 0x2000, v100
	v_add_u32_e32 v102, 0x4000, v100
	v_add_u32_e32 v103, 0x6000, v100
	v_add_u32_e32 v104, 0x8000, v100
	v_add_u32_e32 v105, 0xa000, v100
	v_add_u32_e32 v106, 0xc000, v100
	v_add_u32_e32 v107, 0xe000, v100
	v_mul_u32_u24_e32 v108, 0xe000, v99
	v_lshl_add_u32 v108, v98, 4, v108
	v_add_u32_e32 v109, 0x3800, v108
	v_add_u32_e32 v110, 0x7000, v108
	v_add_u32_e32 v111, 0xa800, v108
	v_mov_b32_e32 v112, 0x20088
	v_mov_b32_e32 v113, 0x200c8
	ds_read_b64 v[114:115], v112
	ds_read_b64 v[116:117], v113
	s_waitcnt lgkmcnt(0)
	v_readfirstlane_b32 s4, v114
	v_readfirstlane_b32 s5, v115
	v_readfirstlane_b32 s6, v116
	v_readfirstlane_b32 s7, v117
	s_sub_i32 s3, s90, 216
	s_lshl_b32 s3, s3, 3
	s_add_i32 s3, s3, s2
	s_add_i32 s3, s3, 0x2e400
	s_nop 4
	s_min_u32 s12, s3, 0x324ff
	s_sub_u32 s12, s12, 0x24500
	s_lshr_b32 s13, s12, 10
	s_mul_i32 s13, s13, 37
	s_lshr_b32 s13, s13, 8
	s_mul_i32 s28, s13, 0x1c00
	s_sub_u32 s12, s12, s28
	s_bfe_u32 s28, s12, 0x50001
	s_and_b32 s32, s12, 1
	s_lshr_b32 s12, s12, 6
	s_lshl_b32 s12, s12, 1
	s_or_b32 s12, s12, s32
	s_mul_i32 s29, s13, 0x3800000
	s_lshl_b32 s32, s12, 18
	s_add_u32 s29, s29, s32
	s_lshl_b32 s32, s28, 8
	s_add_u32 s29, s29, s32
	s_add_u32 s8, s4, s29
	s_addc_u32 s9, s5, 0
	s_mul_i32 s29, s13, 0x1c00000
	s_mul_i32 s32, s28, 0xe0000
	s_add_u32 s29, s29, s32
	s_lshl_b32 s32, s12, 6
	s_add_u32 s29, s29, s32
	s_add_u32 s10, s6, s29
	s_addc_u32 s11, s7, 0
	s_nop 0
	global_load_dwordx4 v[128:131], v100, s[8:9] nt
	global_load_dwordx4 v[132:135], v101, s[8:9] nt
	global_load_dwordx4 v[136:139], v102, s[8:9] nt
	global_load_dwordx4 v[140:143], v103, s[8:9] nt
	global_load_dwordx4 v[144:147], v104, s[8:9] nt
	global_load_dwordx4 v[148:151], v105, s[8:9] nt
	global_load_dwordx4 v[152:155], v106, s[8:9] nt
	global_load_dwordx4 v[156:159], v107, s[8:9] nt
	s_add_i32 s3, s3, 320
	s_min_u32 s12, s3, 0x324ff
	s_sub_u32 s12, s12, 0x24500
	s_lshr_b32 s13, s12, 10
	s_mul_i32 s13, s13, 37
	s_lshr_b32 s13, s13, 8
	s_mul_i32 s28, s13, 0x1c00
	s_sub_u32 s12, s12, s28
	s_bfe_u32 s28, s12, 0x50001
	s_and_b32 s32, s12, 1
	s_lshr_b32 s12, s12, 6
	s_lshl_b32 s12, s12, 1
	s_or_b32 s12, s12, s32
	s_mul_i32 s29, s13, 0x3800000
	s_lshl_b32 s32, s12, 18
	s_add_u32 s29, s29, s32
	s_lshl_b32 s32, s28, 8
	s_add_u32 s29, s29, s32
	s_add_u32 s8, s4, s29
	s_addc_u32 s9, s5, 0
	s_mul_i32 s29, s13, 0x1c00000
	s_mul_i32 s32, s28, 0xe0000
	s_add_u32 s29, s29, s32
	s_lshl_b32 s32, s12, 6
	s_add_u32 s29, s29, s32
	s_add_u32 s36, s6, s29
	s_addc_u32 s37, s7, 0
	s_nop 0
	global_load_dwordx4 v[64:67], v100, s[8:9] nt
	global_load_dwordx4 v[68:71], v101, s[8:9] nt
	global_load_dwordx4 v[72:75], v102, s[8:9] nt
	global_load_dwordx4 v[76:79], v103, s[8:9] nt
	global_load_dwordx4 v[80:83], v104, s[8:9] nt
	global_load_dwordx4 v[84:87], v105, s[8:9] nt
	global_load_dwordx4 v[88:91], v106, s[8:9] nt
	global_load_dwordx4 v[92:95], v107, s[8:9] nt
	s_waitcnt vmcnt(8)
	v_cvt_pk_bf16_f32 v112, v128, v132
	v_cvt_pk_bf16_f32 v113, v136, v140
	v_cvt_pk_bf16_f32 v114, v144, v148
	v_cvt_pk_bf16_f32 v115, v152, v156
	global_store_dwordx4 v108, v[112:115], s[10:11]
	v_cvt_pk_bf16_f32 v116, v129, v133
	v_cvt_pk_bf16_f32 v117, v137, v141
	v_cvt_pk_bf16_f32 v118, v145, v149
	v_cvt_pk_bf16_f32 v119, v153, v157
	global_store_dwordx4 v109, v[116:119], s[10:11]
	v_cvt_pk_bf16_f32 v120, v130, v134
	v_cvt_pk_bf16_f32 v121, v138, v142
	v_cvt_pk_bf16_f32 v122, v146, v150
	v_cvt_pk_bf16_f32 v123, v154, v158
	global_store_dwordx4 v110, v[120:123], s[10:11]
	v_cvt_pk_bf16_f32 v96, v131, v135
	v_cvt_pk_bf16_f32 v97, v139, v143
	v_cvt_pk_bf16_f32 v98, v147, v151
	v_cvt_pk_bf16_f32 v99, v155, v159
	global_store_dwordx4 v111, v[96:99], s[10:11]
	s_movk_i32 s33, 25
; __device__ __forceinline__ ConvTile conv_tile_desc(const unsigned long long* tab, int t) {
;     ...
;     else { const int u = (t < CT_TOTAL ? t : CT_TOTAL - 1) - CT_C; e = u / 7168; const int v = u % 7168; si = 9; di = 17; N = DM; K = EXD; nb = v & 31; kb = v >> 5; }
;     const int n0 = nb * 64;
;     int col0 = n0, nvalid = 64;
;     if (mode) { col0 = (n0 >> 8) * 128 + (n0 & 127); si += (n0 >> 7) & 1; }
;     if (npad) { nvalid = N - n0; if (nvalid <= 0) col0 = 0; }
;     ConvTile c;
;     const size_t KN = (size_t)K * N;
;     c.src = (const float*)tab[si] + (size_t)e * KN + (size_t)(kb * 32) * N + col0;
;     c.dst = (bf16_t*)tab[di] + (size_t)e * (mode ? 2 * KN : KN) + (size_t)n0 * K + kb * 32;
;     c.N = N; c.K = K; c.nvalid = nvalid;
;     return c;
; }
.Lcv1_loop:
	s_add_i32 s3, s3, 320
	s_min_u32 s12, s3, 0x324ff
	s_sub_u32 s12, s12, 0x24500
	s_lshr_b32 s13, s12, 10
	s_mul_i32 s13, s13, 37
	s_lshr_b32 s13, s13, 8
	s_mul_i32 s28, s13, 0x1c00
	s_sub_u32 s12, s12, s28
	s_bfe_u32 s28, s12, 0x50001
	s_and_b32 s32, s12, 1
	s_lshr_b32 s12, s12, 6
	s_lshl_b32 s12, s12, 1
	s_or_b32 s12, s12, s32
	s_mul_i32 s29, s13, 0x3800000
	s_lshl_b32 s32, s12, 18
	s_add_u32 s29, s29, s32
	s_lshl_b32 s32, s28, 8
	s_add_u32 s29, s29, s32
	s_add_u32 s8, s4, s29
	s_addc_u32 s9, s5, 0
	s_mul_i32 s29, s13, 0x1c00000
	s_mul_i32 s32, s28, 0xe0000
	s_add_u32 s29, s29, s32
	s_lshl_b32 s32, s12, 6
	s_add_u32 s29, s29, s32
	s_add_u32 s10, s6, s29
	s_addc_u32 s11, s7, 0
	s_nop 0
	global_load_dwordx4 v[128:131], v100, s[8:9] nt
	global_load_dwordx4 v[132:135], v101, s[8:9] nt
	global_load_dwordx4 v[136:139], v102, s[8:9] nt
	global_load_dwordx4 v[140:143], v103, s[8:9] nt
	global_load_dwordx4 v[144:147], v104, s[8:9] nt
	global_load_dwordx4 v[148:151], v105, s[8:9] nt
	global_load_dwordx4 v[152:155], v106, s[8:9] nt
	global_load_dwordx4 v[156:159], v107, s[8:9] nt
	s_waitcnt vmcnt(12)
	v_cvt_pk_bf16_f32 v112, v64, v68
	v_cvt_pk_bf16_f32 v113, v72, v76
	v_cvt_pk_bf16_f32 v114, v80, v84
	v_cvt_pk_bf16_f32 v115, v88, v92
	global_store_dwordx4 v108, v[112:115], s[36:37]
	v_cvt_pk_bf16_f32 v116, v65, v69
	v_cvt_pk_bf16_f32 v117, v73, v77
	v_cvt_pk_bf16_f32 v118, v81, v85
	v_cvt_pk_bf16_f32 v119, v89, v93
	global_store_dwordx4 v109, v[116:119], s[36:37]
	v_cvt_pk_bf16_f32 v120, v66, v70
	v_cvt_pk_bf16_f32 v121, v74, v78
	v_cvt_pk_bf16_f32 v122, v82, v86
	v_cvt_pk_bf16_f32 v123, v90, v94
	global_store_dwordx4 v110, v[120:123], s[36:37]
	v_cvt_pk_bf16_f32 v96, v67, v71
	v_cvt_pk_bf16_f32 v97, v75, v79
	v_cvt_pk_bf16_f32 v98, v83, v87
	v_cvt_pk_bf16_f32 v99, v91, v95
	global_store_dwordx4 v111, v[96:99], s[36:37]
	s_add_i32 s3, s3, 320
	s_min_u32 s12, s3, 0x324ff
	s_sub_u32 s12, s12, 0x24500
	s_lshr_b32 s13, s12, 10
	s_mul_i32 s13, s13, 37
	s_lshr_b32 s13, s13, 8
	s_mul_i32 s28, s13, 0x1c00
	s_sub_u32 s12, s12, s28
	s_bfe_u32 s28, s12, 0x50001
	s_and_b32 s32, s12, 1
	s_lshr_b32 s12, s12, 6
	s_lshl_b32 s12, s12, 1
	s_or_b32 s12, s12, s32
	s_mul_i32 s29, s13, 0x3800000
	s_lshl_b32 s32, s12, 18
	s_add_u32 s29, s29, s32
	s_lshl_b32 s32, s28, 8
	s_add_u32 s29, s29, s32
	s_add_u32 s8, s4, s29
	s_addc_u32 s9, s5, 0
	s_mul_i32 s29, s13, 0x1c00000
	s_mul_i32 s32, s28, 0xe0000
	s_add_u32 s29, s29, s32
	s_lshl_b32 s32, s12, 6
	s_add_u32 s29, s29, s32
	s_add_u32 s36, s6, s29
	s_addc_u32 s37, s7, 0
	s_nop 0
	global_load_dwordx4 v[64:67], v100, s[8:9] nt
	global_load_dwordx4 v[68:71], v101, s[8:9] nt
	global_load_dwordx4 v[72:75], v102, s[8:9] nt
	global_load_dwordx4 v[76:79], v103, s[8:9] nt
	global_load_dwordx4 v[80:83], v104, s[8:9] nt
	global_load_dwordx4 v[84:87], v105, s[8:9] nt
	global_load_dwordx4 v[88:91], v106, s[8:9] nt
	global_load_dwordx4 v[92:95], v107, s[8:9] nt
	s_waitcnt vmcnt(12)
	v_cvt_pk_bf16_f32 v112, v128, v132
	v_cvt_pk_bf16_f32 v113, v136, v140
	v_cvt_pk_bf16_f32 v114, v144, v148
	v_cvt_pk_bf16_f32 v115, v152, v156
	global_store_dwordx4 v108, v[112:115], s[10:11]
	v_cvt_pk_bf16_f32 v116, v129, v133
	v_cvt_pk_bf16_f32 v117, v137, v141
	v_cvt_pk_bf16_f32 v118, v145, v149
	v_cvt_pk_bf16_f32 v119, v153, v157
	global_store_dwordx4 v109, v[116:119], s[10:11]
	v_cvt_pk_bf16_f32 v120, v130, v134
	v_cvt_pk_bf16_f32 v121, v138, v142
	v_cvt_pk_bf16_f32 v122, v146, v150
	v_cvt_pk_bf16_f32 v123, v154, v158
	global_store_dwordx4 v110, v[120:123], s[10:11]
	v_cvt_pk_bf16_f32 v96, v131, v135
	v_cvt_pk_bf16_f32 v97, v139, v143
	v_cvt_pk_bf16_f32 v98, v147, v151
	v_cvt_pk_bf16_f32 v99, v155, v159
	global_store_dwordx4 v111, v[96:99], s[10:11]
	s_sub_i32 s33, s33, 1
	s_cmp_lg_u32 s33, 0
	s_cbranch_scc1 .Lcv1_loop
	s_waitcnt vmcnt(4)
	v_cvt_pk_bf16_f32 v112, v64, v68
	v_cvt_pk_bf16_f32 v113, v72, v76
	v_cvt_pk_bf16_f32 v114, v80, v84
	v_cvt_pk_bf16_f32 v115, v88, v92
	global_store_dwordx4 v108, v[112:115], s[36:37]
	v_cvt_pk_bf16_f32 v116, v65, v69
	v_cvt_pk_bf16_f32 v117, v73, v77
	v_cvt_pk_bf16_f32 v118, v81, v85
	v_cvt_pk_bf16_f32 v119, v89, v93
	global_store_dwordx4 v109, v[116:119], s[36:37]
	v_cvt_pk_bf16_f32 v120, v66, v70
	v_cvt_pk_bf16_f32 v121, v74, v78
	v_cvt_pk_bf16_f32 v122, v82, v86
	v_cvt_pk_bf16_f32 v123, v90, v94
	global_store_dwordx4 v110, v[120:123], s[36:37]
	v_cvt_pk_bf16_f32 v96, v67, v71
	v_cvt_pk_bf16_f32 v97, v75, v79
	v_cvt_pk_bf16_f32 v98, v83, v87
	v_cvt_pk_bf16_f32 v99, v91, v95
	global_store_dwordx4 v111, v[96:99], s[36:37]
	s_branch .LBB0_1389
